# P5 mid(): touch all 32 gate lines first so only one of the six load rounds pays HBM latency
# baseline (speedup 1.0000x reference)
.LBB0_760:
	s_cmpk_lg_i32 s26, 0x400
	s_cbranch_scc1 .LBB0_762
	s_mov_b64 s[98:99], exec
	s_mov_b64 exec, 0xffff
	v_add_u32_e32 v176, s13, v1
	v_lshlrev_b32_e32 v176, 11, v176
	v_lshl_add_u32 v176, v208, 1, v176
	global_load_dword v179, v176, s[4:5]
	global_load_dword v179, v176, s[2:3]
	global_load_dword v179, v176, s[4:5] offset:256
	global_load_dword v179, v176, s[2:3] offset:256
	v_add_u32_e32 v176, s63, v1
	v_lshlrev_b32_e32 v176, 11, v176
	v_lshl_add_u32 v176, v208, 1, v176
	global_load_dword v179, v176, s[4:5]
	global_load_dword v179, v176, s[2:3]
	global_load_dword v179, v176, s[4:5] offset:256
	global_load_dword v179, v176, s[2:3] offset:256
	v_add_u32_e32 v176, s64, v1
	v_lshlrev_b32_e32 v176, 11, v176
	v_lshl_add_u32 v176, v208, 1, v176
	global_load_dword v179, v176, s[4:5]
	global_load_dword v179, v176, s[2:3]
	global_load_dword v179, v176, s[4:5] offset:256
	global_load_dword v179, v176, s[2:3] offset:256
	v_add_u32_e32 v176, s65, v1
	v_lshlrev_b32_e32 v176, 11, v176
	v_lshl_add_u32 v176, v208, 1, v176
	global_load_dword v179, v176, s[4:5]
	global_load_dword v179, v176, s[2:3]
	global_load_dword v179, v176, s[4:5] offset:256
	global_load_dword v179, v176, s[2:3] offset:256
	v_add_u32_e32 v176, s66, v1
	v_lshlrev_b32_e32 v176, 11, v176
	v_lshl_add_u32 v176, v208, 1, v176
	global_load_dword v179, v176, s[4:5]
	global_load_dword v179, v176, s[2:3]
	global_load_dword v179, v176, s[4:5] offset:256
	global_load_dword v179, v176, s[2:3] offset:256
	v_add_u32_e32 v176, s67, v1
	v_lshlrev_b32_e32 v176, 11, v176
	v_lshl_add_u32 v176, v208, 1, v176
	global_load_dword v179, v176, s[4:5]
	global_load_dword v179, v176, s[2:3]
	global_load_dword v179, v176, s[4:5] offset:256
	global_load_dword v179, v176, s[2:3] offset:256
	v_add_u32_e32 v176, s68, v1
	v_lshlrev_b32_e32 v176, 11, v176
	v_lshl_add_u32 v176, v208, 1, v176
	global_load_dword v179, v176, s[4:5]
	global_load_dword v179, v176, s[2:3]
	global_load_dword v179, v176, s[4:5] offset:256
	global_load_dword v179, v176, s[2:3] offset:256
	v_add_u32_e32 v176, s69, v1
	v_lshlrev_b32_e32 v176, 11, v176
	v_lshl_add_u32 v176, v208, 1, v176
	global_load_dword v179, v176, s[4:5]
	global_load_dword v179, v176, s[2:3]
	global_load_dword v179, v176, s[4:5] offset:256
	global_load_dword v179, v176, s[2:3] offset:256
	s_mov_b64 exec, s[98:99]
	v_mov_b32_e32 v130, 0
	s_nop 0
	v_add_u32_e32 v138, v130, v1
	v_add_u32_e32 v130, s13, v138
	v_ashrrev_i32_e32 v131, 31, v130
	v_lshlrev_b64 v[130:131], 10, v[130:131]
	v_lshl_add_u64 v[130:131], v[130:131], 0, v[208:209]
	v_lshlrev_b64 v[144:145], 1, v[130:131]
	v_lshl_add_u64 v[130:131], s[4:5], 0, v[144:145]
	global_load_dwordx4 v[134:137], v[130:131], off
	v_lshl_add_u64 v[130:131], s[2:3], 0, v[144:145]
	v_or_b32_e32 v144, 0x100, v144
	v_lshl_add_u64 v[140:141], s[4:5], 0, v[144:145]
	global_load_dwordx4 v[130:133], v[130:131], off
	v_lshl_add_u64 v[144:145], s[2:3], 0, v[144:145]
	global_load_dwordx4 v[140:143], v[140:141], off
	v_add_u32_e32 v148, s63, v138
	global_load_dwordx4 v[144:147], v[144:145], off
	v_ashrrev_i32_e32 v149, 31, v148
	v_lshlrev_b64 v[148:149], 10, v[148:149]
	v_lshl_add_u64 v[148:149], v[148:149], 0, v[208:209]
	v_lshlrev_b64 v[156:157], 1, v[148:149]
	v_lshl_add_u64 v[148:149], s[2:3], 0, v[156:157]
	v_lshl_add_u64 v[152:153], s[4:5], 0, v[156:157]
	global_load_dwordx4 v[148:151], v[148:149], off
	s_nop 0
	global_load_dwordx4 v[152:155], v[152:153], off
	v_or_b32_e32 v156, 0x100, v156
	v_lshl_add_u64 v[158:159], s[2:3], 0, v[156:157]
	v_lshl_add_u64 v[160:161], s[4:5], 0, v[156:157]
	global_load_dwordx4 v[156:159], v[158:159], off
	s_nop 0
	global_load_dwordx4 v[160:163], v[160:161], off
	s_waitcnt vmcnt(0)
	v_lshlrev_b32_e32 v139, 16, v134
	v_lshlrev_b32_e32 v168, 16, v135
	v_and_b32_e32 v169, 0xffff0000, v135
	v_rcp_f32_e32 v164, v139
	v_rcp_f32_e32 v168, v168
	v_rcp_f32_e32 v169, v169
	v_lshlrev_b32_e32 v139, 16, v140
	v_and_b32_e32 v173, 0xffff0000, v140
	v_rcp_f32_e32 v172, v139
	v_rcp_f32_e32 v173, v173
	v_and_b32_e32 v165, 0xffff0000, v134
	v_lshlrev_b32_e32 v134, 16, v130
	v_and_b32_e32 v135, 0xffff0000, v130
	v_lshlrev_b32_e32 v130, 16, v131
	v_and_b32_e32 v131, 0xffff0000, v131
	v_lshlrev_b32_e32 v176, 16, v141
	v_and_b32_e32 v177, 0xffff0000, v141
	v_lshlrev_b32_e32 v140, 16, v144
	v_and_b32_e32 v141, 0xffff0000, v144
	v_pk_mul_f32 v[130:131], v[168:169], v[130:131]
	v_lshlrev_b32_e32 v166, 16, v136
	v_and_b32_e32 v167, 0xffff0000, v136
	v_lshlrev_b32_e32 v170, 16, v137
	v_and_b32_e32 v171, 0xffff0000, v137
	v_rcp_f32_e32 v165, v165
	v_pk_mul_f32 v[128:129], v[128:129], v[130:131]
	v_pk_mul_f32 v[130:131], v[172:173], v[140:141]
	v_rcp_f32_e32 v166, v166
	v_rcp_f32_e32 v167, v167
	v_rcp_f32_e32 v170, v170
	v_rcp_f32_e32 v171, v171
	v_lshlrev_b32_e32 v174, 16, v142
	v_and_b32_e32 v175, 0xffff0000, v142
	v_lshlrev_b32_e32 v178, 16, v143
	v_and_b32_e32 v179, 0xffff0000, v143
	v_rcp_f32_e32 v176, v176
	v_rcp_f32_e32 v177, v177
	v_pk_mul_f32 v[94:95], v[94:95], v[130:131]
	v_add_u32_e32 v130, s64, v138
	v_rcp_f32_e32 v174, v174
	v_rcp_f32_e32 v175, v175
	v_rcp_f32_e32 v178, v178
	v_rcp_f32_e32 v179, v179
	v_ashrrev_i32_e32 v131, 31, v130
	v_lshlrev_b64 v[130:131], 10, v[130:131]
	v_lshlrev_b32_e32 v136, 16, v132
	v_and_b32_e32 v137, 0xffff0000, v132
	v_lshlrev_b32_e32 v132, 16, v133
	v_and_b32_e32 v133, 0xffff0000, v133
	v_lshlrev_b32_e32 v144, 16, v145
	v_and_b32_e32 v145, 0xffff0000, v145
	v_pk_mul_f32 v[134:135], v[164:165], v[134:135]
	v_lshl_add_u64 v[130:131], v[130:131], 0, v[208:209]
	v_lshlrev_b32_e32 v142, 16, v146
	v_and_b32_e32 v143, 0xffff0000, v146
	v_lshlrev_b32_e32 v146, 16, v147
	v_and_b32_e32 v147, 0xffff0000, v147
	v_pk_mul_f32 v[136:137], v[166:167], v[136:137]
	v_pk_mul_f32 v[132:133], v[170:171], v[132:133]
	v_pk_mul_f32 v[126:127], v[126:127], v[134:135]
	v_pk_mul_f32 v[134:135], v[176:177], v[144:145]
	v_lshlrev_b64 v[140:141], 1, v[130:131]
	v_pk_mul_f32 v[122:123], v[122:123], v[136:137]
	v_pk_mul_f32 v[124:125], v[124:125], v[132:133]
	v_pk_mul_f32 v[132:133], v[174:175], v[142:143]
	v_pk_mul_f32 v[136:137], v[178:179], v[146:147]
	v_pk_mul_f32 v[96:97], v[96:97], v[134:135]
	v_lshl_add_u64 v[130:131], s[2:3], 0, v[140:141]
	v_lshl_add_u64 v[134:135], s[4:5], 0, v[140:141]
	v_pk_mul_f32 v[90:91], v[90:91], v[132:133]
	v_pk_mul_f32 v[92:93], v[92:93], v[136:137]
	global_load_dwordx4 v[130:133], v[130:131], off
	s_nop 0
	global_load_dwordx4 v[134:137], v[134:135], off
	v_lshlrev_b32_e32 v139, 16, v152
	v_and_b32_e32 v143, 0xffff0000, v152
	v_rcp_f32_e32 v142, v139
	v_rcp_f32_e32 v143, v143
	v_lshlrev_b32_e32 v144, 16, v154
	v_and_b32_e32 v145, 0xffff0000, v154
	v_rcp_f32_e32 v144, v144
	v_rcp_f32_e32 v145, v145
	v_lshlrev_b32_e32 v146, 16, v148
	v_and_b32_e32 v147, 0xffff0000, v148
	v_pk_mul_f32 v[142:143], v[142:143], v[146:147]
	v_lshlrev_b32_e32 v152, 16, v153
	v_pk_mul_f32 v[118:119], v[118:119], v[142:143]
	v_lshlrev_b32_e32 v142, 16, v150
	v_and_b32_e32 v143, 0xffff0000, v150
	v_and_b32_e32 v153, 0xffff0000, v153
	v_pk_mul_f32 v[142:143], v[144:145], v[142:143]
	v_lshlrev_b32_e32 v154, 16, v155
	v_pk_mul_f32 v[114:115], v[114:115], v[142:143]
	v_rcp_f32_e32 v142, v152
	v_rcp_f32_e32 v143, v153
	v_and_b32_e32 v155, 0xffff0000, v155
	v_rcp_f32_e32 v144, v154
	v_rcp_f32_e32 v145, v155
	v_lshlrev_b32_e32 v146, 16, v149
	v_and_b32_e32 v147, 0xffff0000, v149
	v_pk_mul_f32 v[142:143], v[142:143], v[146:147]
	v_or_b32_e32 v140, 0x100, v140
	v_pk_mul_f32 v[120:121], v[120:121], v[142:143]
	v_lshlrev_b32_e32 v142, 16, v151
	v_and_b32_e32 v143, 0xffff0000, v151
	v_pk_mul_f32 v[142:143], v[144:145], v[142:143]
	v_lshl_add_u64 v[144:145], s[4:5], 0, v[140:141]
	v_pk_mul_f32 v[116:117], v[116:117], v[142:143]
	v_lshl_add_u64 v[142:143], s[2:3], 0, v[140:141]
	v_lshlrev_b32_e32 v139, 16, v160
	v_and_b32_e32 v149, 0xffff0000, v160
	global_load_dwordx4 v[140:143], v[142:143], off
	s_nop 0
	global_load_dwordx4 v[144:147], v[144:145], off
	v_rcp_f32_e32 v148, v139
	v_rcp_f32_e32 v149, v149
	v_lshlrev_b32_e32 v150, 16, v162
	v_and_b32_e32 v151, 0xffff0000, v162
	v_rcp_f32_e32 v150, v150
	v_rcp_f32_e32 v151, v151
	v_lshlrev_b32_e32 v152, 16, v156
	v_and_b32_e32 v153, 0xffff0000, v156
	v_pk_mul_f32 v[148:149], v[148:149], v[152:153]
	v_lshlrev_b32_e32 v154, 16, v161
	v_pk_mul_f32 v[86:87], v[86:87], v[148:149]
	v_lshlrev_b32_e32 v148, 16, v158
	v_and_b32_e32 v149, 0xffff0000, v158
	v_and_b32_e32 v155, 0xffff0000, v161
	v_pk_mul_f32 v[148:149], v[150:151], v[148:149]
	v_lshlrev_b32_e32 v160, 16, v163
	v_pk_mul_f32 v[82:83], v[82:83], v[148:149]
	v_rcp_f32_e32 v148, v154
	v_rcp_f32_e32 v149, v155
	v_and_b32_e32 v161, 0xffff0000, v163
	v_rcp_f32_e32 v150, v160
	v_rcp_f32_e32 v151, v161
	v_lshlrev_b32_e32 v152, 16, v157
	v_and_b32_e32 v153, 0xffff0000, v157
	v_pk_mul_f32 v[148:149], v[148:149], v[152:153]
	s_waitcnt vmcnt(0)
	v_lshlrev_b32_e32 v139, 16, v134
	v_pk_mul_f32 v[88:89], v[88:89], v[148:149]
	v_lshlrev_b32_e32 v148, 16, v159
	v_and_b32_e32 v149, 0xffff0000, v159
	v_pk_mul_f32 v[148:149], v[150:151], v[148:149]
	v_and_b32_e32 v158, 0xffff0000, v134
	v_pk_mul_f32 v[84:85], v[84:85], v[148:149]
	v_add_u32_e32 v148, s65, v138
	v_ashrrev_i32_e32 v149, 31, v148
	v_lshlrev_b64 v[148:149], 10, v[148:149]
	v_lshl_add_u64 v[148:149], v[148:149], 0, v[208:209]
	v_lshlrev_b64 v[156:157], 1, v[148:149]
	v_lshl_add_u64 v[148:149], s[2:3], 0, v[156:157]
	v_lshl_add_u64 v[152:153], s[4:5], 0, v[156:157]
	global_load_dwordx4 v[148:151], v[148:149], off
	s_nop 0
	global_load_dwordx4 v[152:155], v[152:153], off
	v_lshlrev_b32_e32 v160, 16, v135
	v_and_b32_e32 v161, 0xffff0000, v135
	v_rcp_f32_e32 v134, v139
	v_rcp_f32_e32 v135, v158
	v_lshlrev_b32_e32 v159, 16, v136
	v_and_b32_e32 v162, 0xffff0000, v136
	v_lshlrev_b32_e32 v163, 16, v137
	v_and_b32_e32 v164, 0xffff0000, v137
	v_rcp_f32_e32 v136, v159
	v_rcp_f32_e32 v137, v162
	v_lshlrev_b32_e32 v158, 16, v130
	v_and_b32_e32 v159, 0xffff0000, v130
	v_pk_mul_f32 v[134:135], v[134:135], v[158:159]
	v_rcp_f32_e32 v130, v163
	v_pk_mul_f32 v[110:111], v[110:111], v[134:135]
	v_lshlrev_b32_e32 v134, 16, v132
	v_and_b32_e32 v135, 0xffff0000, v132
	v_pk_mul_f32 v[134:135], v[136:137], v[134:135]
	v_lshlrev_b32_e32 v136, 16, v131
	v_pk_mul_f32 v[106:107], v[106:107], v[134:135]
	v_rcp_f32_e32 v134, v160
	v_rcp_f32_e32 v135, v161
	v_and_b32_e32 v137, 0xffff0000, v131
	v_rcp_f32_e32 v131, v164
	v_lshlrev_b32_e32 v132, 16, v133
	v_and_b32_e32 v133, 0xffff0000, v133
	v_pk_mul_f32 v[134:135], v[134:135], v[136:137]
	v_pk_mul_f32 v[130:131], v[130:131], v[132:133]
	v_or_b32_e32 v156, 0x100, v156
	v_pk_mul_f32 v[112:113], v[112:113], v[134:135]
	v_pk_mul_f32 v[108:109], v[108:109], v[130:131]
	v_lshl_add_u64 v[130:131], s[2:3], 0, v[156:157]
	v_lshl_add_u64 v[134:135], s[4:5], 0, v[156:157]
	global_load_dwordx4 v[130:133], v[130:131], off
	s_nop 0
	global_load_dwordx4 v[134:137], v[134:135], off
	v_lshlrev_b32_e32 v139, 16, v144
	v_and_b32_e32 v156, 0xffff0000, v144
	v_lshlrev_b32_e32 v158, 16, v145
	v_and_b32_e32 v159, 0xffff0000, v145
	v_rcp_f32_e32 v144, v139
	v_rcp_f32_e32 v145, v156
	v_lshlrev_b32_e32 v157, 16, v146
	v_and_b32_e32 v160, 0xffff0000, v146
	v_lshlrev_b32_e32 v161, 16, v147
	v_and_b32_e32 v162, 0xffff0000, v147
	v_rcp_f32_e32 v146, v157
	v_rcp_f32_e32 v147, v160
	v_lshlrev_b32_e32 v156, 16, v140
	v_and_b32_e32 v157, 0xffff0000, v140
	v_pk_mul_f32 v[144:145], v[144:145], v[156:157]
	v_rcp_f32_e32 v140, v161
	v_pk_mul_f32 v[78:79], v[78:79], v[144:145]
	v_lshlrev_b32_e32 v144, 16, v142
	v_and_b32_e32 v145, 0xffff0000, v142
	v_pk_mul_f32 v[144:145], v[146:147], v[144:145]
	v_lshlrev_b32_e32 v146, 16, v141
	v_and_b32_e32 v147, 0xffff0000, v141
	v_rcp_f32_e32 v141, v162
	v_lshlrev_b32_e32 v142, 16, v143
	v_and_b32_e32 v143, 0xffff0000, v143
	v_pk_mul_f32 v[74:75], v[74:75], v[144:145]
	v_pk_mul_f32 v[140:141], v[140:141], v[142:143]
	v_rcp_f32_e32 v144, v158
	v_rcp_f32_e32 v145, v159
	v_pk_mul_f32 v[76:77], v[76:77], v[140:141]
	v_add_u32_e32 v140, s66, v138
	v_ashrrev_i32_e32 v141, 31, v140
	v_lshlrev_b64 v[140:141], 10, v[140:141]
	v_lshl_add_u64 v[140:141], v[140:141], 0, v[208:209]
	v_pk_mul_f32 v[144:145], v[144:145], v[146:147]
	v_lshlrev_b64 v[156:157], 1, v[140:141]
	v_pk_mul_f32 v[80:81], v[80:81], v[144:145]
	v_lshl_add_u64 v[140:141], s[2:3], 0, v[156:157]
	v_lshl_add_u64 v[144:145], s[4:5], 0, v[156:157]
	global_load_dwordx4 v[140:143], v[140:141], off
	s_nop 0
	global_load_dwordx4 v[144:147], v[144:145], off
	v_or_b32_e32 v156, 0x100, v156
	s_waitcnt vmcnt(0)
	v_lshlrev_b32_e32 v139, 16, v152
	v_and_b32_e32 v158, 0xffff0000, v152
	v_lshlrev_b32_e32 v160, 16, v153
	v_and_b32_e32 v161, 0xffff0000, v153
	v_rcp_f32_e32 v152, v139
	v_rcp_f32_e32 v153, v158
	v_lshlrev_b32_e32 v159, 16, v154
	v_and_b32_e32 v162, 0xffff0000, v154
	v_lshlrev_b32_e32 v163, 16, v155
	v_and_b32_e32 v164, 0xffff0000, v155
	v_rcp_f32_e32 v154, v159
	v_rcp_f32_e32 v155, v162
	v_lshlrev_b32_e32 v158, 16, v148
	v_and_b32_e32 v159, 0xffff0000, v148
	v_pk_mul_f32 v[152:153], v[152:153], v[158:159]
	v_rcp_f32_e32 v148, v163
	v_pk_mul_f32 v[102:103], v[102:103], v[152:153]
	v_lshlrev_b32_e32 v152, 16, v150
	v_and_b32_e32 v153, 0xffff0000, v150
	v_pk_mul_f32 v[152:153], v[154:155], v[152:153]
	v_lshlrev_b32_e32 v154, 16, v149
	v_pk_mul_f32 v[98:99], v[98:99], v[152:153]
	v_rcp_f32_e32 v152, v160
	v_rcp_f32_e32 v153, v161
	v_and_b32_e32 v155, 0xffff0000, v149
	v_rcp_f32_e32 v149, v164
	v_lshlrev_b32_e32 v150, 16, v151
	v_and_b32_e32 v151, 0xffff0000, v151
	v_pk_mul_f32 v[152:153], v[152:153], v[154:155]
	v_pk_mul_f32 v[148:149], v[148:149], v[150:151]
	v_pk_mul_f32 v[104:105], v[104:105], v[152:153]
	v_pk_mul_f32 v[100:101], v[100:101], v[148:149]
	v_lshl_add_u64 v[148:149], s[2:3], 0, v[156:157]
	v_lshl_add_u64 v[152:153], s[4:5], 0, v[156:157]
	global_load_dwordx4 v[148:151], v[148:149], off
	s_nop 0
	global_load_dwordx4 v[152:155], v[152:153], off
	v_lshlrev_b32_e32 v139, 16, v134
	v_and_b32_e32 v156, 0xffff0000, v134
	v_lshlrev_b32_e32 v158, 16, v135
	v_and_b32_e32 v159, 0xffff0000, v135
	v_rcp_f32_e32 v134, v139
	v_rcp_f32_e32 v135, v156
	v_lshlrev_b32_e32 v157, 16, v136
	v_and_b32_e32 v160, 0xffff0000, v136
	v_lshlrev_b32_e32 v161, 16, v137
	v_and_b32_e32 v162, 0xffff0000, v137
	v_rcp_f32_e32 v136, v157
	v_rcp_f32_e32 v137, v160
	v_lshlrev_b32_e32 v156, 16, v130
	v_and_b32_e32 v157, 0xffff0000, v130
	v_pk_mul_f32 v[134:135], v[134:135], v[156:157]
	v_rcp_f32_e32 v130, v161
	v_pk_mul_f32 v[70:71], v[70:71], v[134:135]
	v_lshlrev_b32_e32 v134, 16, v132
	v_and_b32_e32 v135, 0xffff0000, v132
	v_pk_mul_f32 v[134:135], v[136:137], v[134:135]
	v_lshlrev_b32_e32 v136, 16, v131
	v_and_b32_e32 v137, 0xffff0000, v131
	v_rcp_f32_e32 v131, v162
	v_lshlrev_b32_e32 v132, 16, v133
	v_and_b32_e32 v133, 0xffff0000, v133
	v_pk_mul_f32 v[66:67], v[66:67], v[134:135]
	v_pk_mul_f32 v[130:131], v[130:131], v[132:133]
	v_rcp_f32_e32 v134, v158
	v_pk_mul_f32 v[68:69], v[68:69], v[130:131]
	v_add_u32_e32 v130, s67, v138
	v_rcp_f32_e32 v135, v159
	v_ashrrev_i32_e32 v131, 31, v130
	v_lshlrev_b64 v[130:131], 10, v[130:131]
	v_lshl_add_u64 v[130:131], v[130:131], 0, v[208:209]
	v_lshlrev_b64 v[130:131], 1, v[130:131]
	v_pk_mul_f32 v[134:135], v[134:135], v[136:137]
	v_lshl_add_u64 v[132:133], s[2:3], 0, v[130:131]
	v_pk_mul_f32 v[72:73], v[72:73], v[134:135]
	v_lshl_add_u64 v[134:135], s[4:5], 0, v[130:131]
	global_load_dwordx4 v[156:159], v[132:133], off
	global_load_dwordx4 v[160:163], v[134:135], off
	v_lshlrev_b32_e32 v132, 16, v144
	v_and_b32_e32 v133, 0xffff0000, v144
	v_rcp_f32_e32 v132, v132
	v_rcp_f32_e32 v133, v133
	v_lshlrev_b32_e32 v134, 16, v146
	v_and_b32_e32 v135, 0xffff0000, v146
	v_rcp_f32_e32 v134, v134
	v_rcp_f32_e32 v135, v135
	v_lshlrev_b32_e32 v136, 16, v140
	v_and_b32_e32 v137, 0xffff0000, v140
	v_pk_mul_f32 v[132:133], v[132:133], v[136:137]
	v_lshlrev_b32_e32 v139, 16, v145
	v_pk_mul_f32 v[62:63], v[62:63], v[132:133]
	v_lshlrev_b32_e32 v132, 16, v142
	v_and_b32_e32 v133, 0xffff0000, v142
	v_and_b32_e32 v144, 0xffff0000, v145
	v_pk_mul_f32 v[132:133], v[134:135], v[132:133]
	v_lshlrev_b32_e32 v145, 16, v147
	v_pk_mul_f32 v[58:59], v[58:59], v[132:133]
	v_rcp_f32_e32 v132, v139
	v_rcp_f32_e32 v133, v144
	v_and_b32_e32 v146, 0xffff0000, v147
	v_rcp_f32_e32 v134, v145
	v_rcp_f32_e32 v135, v146
	v_lshlrev_b32_e32 v136, 16, v141
	v_and_b32_e32 v137, 0xffff0000, v141
	v_pk_mul_f32 v[132:133], v[132:133], v[136:137]
	v_or_b32_e32 v130, 0x100, v130
	v_pk_mul_f32 v[64:65], v[64:65], v[132:133]
	v_lshlrev_b32_e32 v132, 16, v143
	v_and_b32_e32 v133, 0xffff0000, v143
	v_pk_mul_f32 v[132:133], v[134:135], v[132:133]
	v_lshl_add_u64 v[134:135], s[4:5], 0, v[130:131]
	v_pk_mul_f32 v[60:61], v[60:61], v[132:133]
	v_lshl_add_u64 v[132:133], s[2:3], 0, v[130:131]
	global_load_dwordx4 v[130:133], v[132:133], off
	s_nop 0
	global_load_dwordx4 v[140:143], v[134:135], off
	s_waitcnt vmcnt(0)
	v_lshlrev_b32_e32 v144, 16, v148
	v_lshlrev_b32_e32 v134, 16, v152
	v_and_b32_e32 v135, 0xffff0000, v152
	v_rcp_f32_e32 v134, v134
	v_rcp_f32_e32 v135, v135
	v_lshlrev_b32_e32 v136, 16, v154
	v_and_b32_e32 v137, 0xffff0000, v154
	v_rcp_f32_e32 v136, v136
	v_rcp_f32_e32 v137, v137
	v_and_b32_e32 v145, 0xffff0000, v148
	v_pk_mul_f32 v[134:135], v[134:135], v[144:145]
	v_lshlrev_b32_e32 v139, 16, v153
	v_pk_mul_f32 v[30:31], v[30:31], v[134:135]
	v_lshlrev_b32_e32 v134, 16, v150
	v_and_b32_e32 v135, 0xffff0000, v150
	v_and_b32_e32 v146, 0xffff0000, v153
	v_pk_mul_f32 v[134:135], v[136:137], v[134:135]
	v_lshlrev_b32_e32 v147, 16, v155
	v_pk_mul_f32 v[26:27], v[26:27], v[134:135]
	v_rcp_f32_e32 v134, v139
	v_rcp_f32_e32 v135, v146
	v_and_b32_e32 v152, 0xffff0000, v155
	v_rcp_f32_e32 v136, v147
	v_rcp_f32_e32 v137, v152
	v_lshlrev_b32_e32 v144, 16, v149
	v_and_b32_e32 v145, 0xffff0000, v149
	v_pk_mul_f32 v[134:135], v[134:135], v[144:145]
	v_lshlrev_b32_e32 v154, 16, v156
	v_pk_mul_f32 v[32:33], v[32:33], v[134:135]
	v_lshlrev_b32_e32 v134, 16, v151
	v_and_b32_e32 v135, 0xffff0000, v151
	v_pk_mul_f32 v[134:135], v[136:137], v[134:135]
	v_lshlrev_b32_e32 v139, 16, v160
	v_pk_mul_f32 v[28:29], v[28:29], v[134:135]
	v_add_u32_e32 v134, s68, v138
	v_ashrrev_i32_e32 v135, 31, v134
	v_lshlrev_b64 v[134:135], 10, v[134:135]
	v_lshl_add_u64 v[134:135], v[134:135], 0, v[208:209]
	v_lshlrev_b64 v[148:149], 1, v[134:135]
	v_lshl_add_u64 v[134:135], s[2:3], 0, v[148:149]
	v_lshl_add_u64 v[144:145], s[4:5], 0, v[148:149]
	global_load_dwordx4 v[134:137], v[134:135], off
	s_nop 0
	global_load_dwordx4 v[144:147], v[144:145], off
	v_and_b32_e32 v151, 0xffff0000, v160
	v_rcp_f32_e32 v150, v139
	v_rcp_f32_e32 v151, v151
	v_lshlrev_b32_e32 v152, 16, v162
	v_and_b32_e32 v153, 0xffff0000, v162
	v_rcp_f32_e32 v152, v152
	v_rcp_f32_e32 v153, v153
	v_and_b32_e32 v155, 0xffff0000, v156
	v_pk_mul_f32 v[150:151], v[150:151], v[154:155]
	v_lshlrev_b32_e32 v160, 16, v161
	v_pk_mul_f32 v[54:55], v[54:55], v[150:151]
	v_lshlrev_b32_e32 v150, 16, v158
	v_and_b32_e32 v151, 0xffff0000, v158
	v_and_b32_e32 v161, 0xffff0000, v161
	v_pk_mul_f32 v[150:151], v[152:153], v[150:151]
	v_lshlrev_b32_e32 v162, 16, v163
	v_pk_mul_f32 v[50:51], v[50:51], v[150:151]
	v_rcp_f32_e32 v150, v160
	v_rcp_f32_e32 v151, v161
	v_and_b32_e32 v163, 0xffff0000, v163
	v_rcp_f32_e32 v152, v162
	v_rcp_f32_e32 v153, v163
	v_lshlrev_b32_e32 v154, 16, v157
	v_and_b32_e32 v155, 0xffff0000, v157
	v_pk_mul_f32 v[150:151], v[150:151], v[154:155]
	v_or_b32_e32 v148, 0x100, v148
	v_pk_mul_f32 v[56:57], v[56:57], v[150:151]
	v_lshlrev_b32_e32 v150, 16, v159
	v_and_b32_e32 v151, 0xffff0000, v159
	v_pk_mul_f32 v[150:151], v[152:153], v[150:151]
	v_lshl_add_u64 v[152:153], s[4:5], 0, v[148:149]
	v_pk_mul_f32 v[52:53], v[52:53], v[150:151]
	v_lshl_add_u64 v[150:151], s[2:3], 0, v[148:149]
	global_load_dwordx4 v[148:151], v[150:151], off
	s_nop 0
	global_load_dwordx4 v[152:155], v[152:153], off
	v_lshlrev_b32_e32 v139, 16, v140
	v_and_b32_e32 v156, 0xffff0000, v140
	v_lshlrev_b32_e32 v158, 16, v141
	v_and_b32_e32 v159, 0xffff0000, v141
	v_rcp_f32_e32 v140, v139
	v_rcp_f32_e32 v141, v156
	v_lshlrev_b32_e32 v157, 16, v142
	v_and_b32_e32 v160, 0xffff0000, v142
	v_add_u32_e32 v138, s69, v138
	v_lshlrev_b32_e32 v162, 16, v143
	v_and_b32_e32 v164, 0xffff0000, v143
	v_rcp_f32_e32 v142, v157
	v_rcp_f32_e32 v143, v160
	v_ashrrev_i32_e32 v139, 31, v138
	v_lshlrev_b32_e32 v156, 16, v130
	v_and_b32_e32 v157, 0xffff0000, v130
	v_lshlrev_b64 v[138:139], 10, v[138:139]
	v_pk_mul_f32 v[140:141], v[140:141], v[156:157]
	v_lshl_add_u64 v[138:139], v[138:139], 0, v[208:209]
	v_pk_mul_f32 v[22:23], v[22:23], v[140:141]
	v_lshlrev_b32_e32 v140, 16, v132
	v_and_b32_e32 v141, 0xffff0000, v132
	v_lshlrev_b64 v[160:161], 1, v[138:139]
	v_pk_mul_f32 v[140:141], v[142:143], v[140:141]
	v_lshl_add_u64 v[138:139], s[2:3], 0, v[160:161]
	v_lshl_add_u64 v[156:157], s[4:5], 0, v[160:161]
	v_pk_mul_f32 v[18:19], v[18:19], v[140:141]
	v_rcp_f32_e32 v142, v158
	v_rcp_f32_e32 v143, v159
	global_load_dwordx4 v[138:141], v[138:139], off
	s_nop 0
	global_load_dwordx4 v[156:159], v[156:157], off
	v_rcp_f32_e32 v130, v162
	v_lshlrev_b32_e32 v162, 16, v131
	v_and_b32_e32 v163, 0xffff0000, v131
	v_rcp_f32_e32 v131, v164
	v_lshlrev_b32_e32 v132, 16, v133
	v_and_b32_e32 v133, 0xffff0000, v133
	v_pk_mul_f32 v[142:143], v[142:143], v[162:163]
	v_pk_mul_f32 v[130:131], v[130:131], v[132:133]
	v_pk_mul_f32 v[24:25], v[24:25], v[142:143]
	v_pk_mul_f32 v[20:21], v[20:21], v[130:131]
	v_or_b32_e32 v160, 0x100, v160
	s_waitcnt vmcnt(0)
	v_and_b32_e32 v133, 0xffff0000, v134
	v_lshlrev_b32_e32 v130, 16, v144
	v_and_b32_e32 v131, 0xffff0000, v144
	v_rcp_f32_e32 v130, v130
	v_rcp_f32_e32 v131, v131
	v_lshlrev_b32_e32 v132, 16, v146
	v_and_b32_e32 v142, 0xffff0000, v146
	v_rcp_f32_e32 v146, v132
	v_lshlrev_b32_e32 v132, 16, v134
	v_pk_mul_f32 v[130:131], v[130:131], v[132:133]
	v_lshlrev_b32_e32 v166, 16, v147
	v_and_b32_e32 v167, 0xffff0000, v147
	v_pk_mul_f32 v[46:47], v[46:47], v[130:131]
	v_rcp_f32_e32 v147, v142
	v_lshl_add_u64 v[130:131], s[2:3], 0, v[160:161]
	v_lshl_add_u64 v[142:143], s[4:5], 0, v[160:161]
	v_lshlrev_b32_e32 v164, 16, v145
	v_and_b32_e32 v165, 0xffff0000, v145
	global_load_dwordx4 v[130:133], v[130:131], off
	s_nop 0
	global_load_dwordx4 v[142:145], v[142:143], off
	v_rcp_f32_e32 v134, v166
	v_lshlrev_b32_e32 v160, 16, v135
	v_and_b32_e32 v161, 0xffff0000, v135
	v_rcp_f32_e32 v135, v167
	v_lshlrev_b32_e32 v162, 16, v136
	v_and_b32_e32 v163, 0xffff0000, v136
	v_pk_mul_f32 v[146:147], v[146:147], v[162:163]
	v_lshlrev_b32_e32 v136, 16, v137
	v_and_b32_e32 v137, 0xffff0000, v137
	v_pk_mul_f32 v[42:43], v[42:43], v[146:147]
	v_rcp_f32_e32 v146, v164
	v_rcp_f32_e32 v147, v165
	v_pk_mul_f32 v[134:135], v[134:135], v[136:137]
	v_pk_mul_f32 v[146:147], v[146:147], v[160:161]
	v_pk_mul_f32 v[44:45], v[44:45], v[134:135]
	v_lshlrev_b32_e32 v134, 16, v152
	v_and_b32_e32 v135, 0xffff0000, v152
	v_rcp_f32_e32 v134, v134
	v_rcp_f32_e32 v135, v135
	v_lshlrev_b32_e32 v136, 16, v154
	v_and_b32_e32 v137, 0xffff0000, v154
	v_rcp_f32_e32 v136, v136
	v_rcp_f32_e32 v137, v137
	v_pk_mul_f32 v[48:49], v[48:49], v[146:147]
	v_lshlrev_b32_e32 v146, 16, v148
	v_and_b32_e32 v147, 0xffff0000, v148
	v_pk_mul_f32 v[134:135], v[134:135], v[146:147]
	v_lshlrev_b32_e32 v152, 16, v153
	v_pk_mul_f32 v[14:15], v[14:15], v[134:135]
	v_lshlrev_b32_e32 v134, 16, v150
	v_and_b32_e32 v135, 0xffff0000, v150
	v_and_b32_e32 v153, 0xffff0000, v153
	v_pk_mul_f32 v[134:135], v[136:137], v[134:135]
	v_lshlrev_b32_e32 v154, 16, v155
	v_pk_mul_f32 v[10:11], v[10:11], v[134:135]
	v_rcp_f32_e32 v134, v152
	v_rcp_f32_e32 v135, v153
	v_and_b32_e32 v155, 0xffff0000, v155
	v_rcp_f32_e32 v136, v154
	v_rcp_f32_e32 v137, v155
	v_lshlrev_b32_e32 v146, 16, v149
	v_and_b32_e32 v147, 0xffff0000, v149
	v_pk_mul_f32 v[134:135], v[134:135], v[146:147]
	v_lshlrev_b32_e32 v146, 16, v138
	v_pk_mul_f32 v[16:17], v[16:17], v[134:135]
	v_lshlrev_b32_e32 v134, 16, v151
	v_and_b32_e32 v135, 0xffff0000, v151
	v_pk_mul_f32 v[134:135], v[136:137], v[134:135]
	v_lshlrev_b32_e32 v136, 16, v158
	v_pk_mul_f32 v[12:13], v[12:13], v[134:135]
	v_lshlrev_b32_e32 v134, 16, v156
	v_and_b32_e32 v135, 0xffff0000, v156
	v_rcp_f32_e32 v134, v134
	v_rcp_f32_e32 v135, v135
	v_and_b32_e32 v137, 0xffff0000, v158
	v_rcp_f32_e32 v136, v136
	v_rcp_f32_e32 v137, v137
	v_and_b32_e32 v147, 0xffff0000, v138
	v_pk_mul_f32 v[134:135], v[134:135], v[146:147]
	v_lshlrev_b32_e32 v148, 16, v157
	v_pk_mul_f32 v[38:39], v[38:39], v[134:135]
	v_lshlrev_b32_e32 v134, 16, v140
	v_and_b32_e32 v135, 0xffff0000, v140
	v_and_b32_e32 v149, 0xffff0000, v157
	v_pk_mul_f32 v[134:135], v[136:137], v[134:135]
	v_lshlrev_b32_e32 v150, 16, v159
	v_pk_mul_f32 v[34:35], v[34:35], v[134:135]
	v_rcp_f32_e32 v134, v148
	v_rcp_f32_e32 v135, v149
	v_and_b32_e32 v151, 0xffff0000, v159
	v_rcp_f32_e32 v136, v150
	v_rcp_f32_e32 v137, v151
	v_lshlrev_b32_e32 v138, 16, v139
	v_and_b32_e32 v139, 0xffff0000, v139
	v_pk_mul_f32 v[134:135], v[134:135], v[138:139]
	s_waitcnt vmcnt(0)
	v_lshlrev_b32_e32 v138, 16, v130
	v_pk_mul_f32 v[40:41], v[40:41], v[134:135]
	v_lshlrev_b32_e32 v134, 16, v141
	v_and_b32_e32 v135, 0xffff0000, v141
	v_pk_mul_f32 v[134:135], v[136:137], v[134:135]
	v_lshlrev_b32_e32 v136, 16, v144
	v_pk_mul_f32 v[36:37], v[36:37], v[134:135]
	v_lshlrev_b32_e32 v134, 16, v142
	v_and_b32_e32 v135, 0xffff0000, v142
	v_rcp_f32_e32 v134, v134
	v_rcp_f32_e32 v135, v135
	v_and_b32_e32 v137, 0xffff0000, v144
	v_rcp_f32_e32 v136, v136
	v_rcp_f32_e32 v137, v137
	v_and_b32_e32 v139, 0xffff0000, v130
	v_pk_mul_f32 v[134:135], v[134:135], v[138:139]
	v_lshlrev_b32_e32 v140, 16, v143
	v_pk_mul_f32 v[6:7], v[6:7], v[134:135]
	v_lshlrev_b32_e32 v134, 16, v132
	v_and_b32_e32 v135, 0xffff0000, v132
	v_and_b32_e32 v141, 0xffff0000, v143
	v_lshlrev_b32_e32 v142, 16, v145
	v_and_b32_e32 v143, 0xffff0000, v145
	v_pk_mul_f32 v[134:135], v[136:137], v[134:135]
	v_rcp_f32_e32 v130, v142
	v_pk_mul_f32 v[2:3], v[2:3], v[134:135]
	v_rcp_f32_e32 v134, v140
	v_rcp_f32_e32 v135, v141
	v_lshlrev_b32_e32 v136, 16, v131
	v_and_b32_e32 v137, 0xffff0000, v131
	v_rcp_f32_e32 v131, v143
	v_lshlrev_b32_e32 v132, 16, v133
	v_and_b32_e32 v133, 0xffff0000, v133
	v_pk_mul_f32 v[134:135], v[134:135], v[136:137]
	v_pk_mul_f32 v[130:131], v[130:131], v[132:133]
	v_pk_mul_f32 v[8:9], v[8:9], v[134:135]
	v_pk_mul_f32 v[4:5], v[4:5], v[130:131]
